# next block's lo/len row prefetched at flush start; rbLast taken with v_readlane instead of a separate ds_read + wait in the re-init
# speedup vs baseline: 1.0023x; 1.0015x over previous
.Lpeel_join:
	v_cmp_ge_i32_e32 vcc, s18, v249
	s_mov_b64 s[8:9], 0
	s_and_saveexec_b64 s[2:3], vcc
	s_cbranch_execz .LBB1_148
	s_setprio 3
	v_cmp_gt_i32_e32 vcc, s12, v235
	s_and_b64 s[10:11], s[0:1], vcc
	v_add_u32_e32 v3, 1, v251
	v_lshl_add_u32 v3, v3, 7, v244
	ds_read2_b32 v[230:231], v3 offset1:1
	ds_read_b128 v[82:85], v245 offset:32768
	ds_read_b128 v[86:89], v245 offset:32784
	ds_read_b128 v[90:93], v245 offset:32800
	ds_read_b128 v[94:97], v245 offset:32816
	ds_read_b128 v[98:101], v245 offset:32832
	ds_read_b128 v[102:105], v245 offset:32848
	ds_read_b128 v[106:109], v245 offset:32864
	ds_read_b128 v[110:113], v245 offset:32880
	ds_read_b128 v[114:117], v246 offset:0
	ds_read_b128 v[118:121], v246 offset:8192
	ds_read_b128 v[122:125], v246 offset:1024
	ds_read_b128 v[126:129], v246 offset:9216
	v_cvt_f32_i32_e32 v16, v234
	v_cvt_pk_f16_f32 v4, v66, v67
	v_cvt_pk_f16_f32 v5, v68, v69
	v_cvt_pk_f16_f32 v6, v70, v71
	v_cvt_pk_f16_f32 v7, v72, v73
	v_cvt_pk_f16_f32 v8, v74, v75
	v_cvt_pk_f16_f32 v9, v76, v77
	v_cvt_pk_f16_f32 v10, v78, v79
	v_cvt_pk_f16_f32 v11, v80, v81
	s_waitcnt lgkmcnt(8)
	v_pk_mul_f32 v[162:163], v[82:83], v[16:17] op_sel_hi:[1,0]
	v_pk_mul_f32 v[164:165], v[84:85], v[16:17] op_sel_hi:[1,0]
	v_pk_mul_f32 v[166:167], v[86:87], v[16:17] op_sel_hi:[1,0]
	v_pk_mul_f32 v[168:169], v[88:89], v[16:17] op_sel_hi:[1,0]
	v_pk_mul_f32 v[170:171], v[90:91], v[16:17] op_sel_hi:[1,0]
	v_pk_mul_f32 v[172:173], v[92:93], v[16:17] op_sel_hi:[1,0]
	v_pk_mul_f32 v[174:175], v[94:95], v[16:17] op_sel_hi:[1,0]
	v_pk_mul_f32 v[176:177], v[96:97], v[16:17] op_sel_hi:[1,0]
	ds_read_b128 v[130:133], v246 offset:2048
	ds_read_b128 v[134:137], v246 offset:10240
	ds_read_b128 v[138:141], v246 offset:3072
	ds_read_b128 v[142:145], v246 offset:11264
	s_waitcnt lgkmcnt(4)
	v_mfma_f32_32x32x16_f16 v[162:177], v[114:117], v[4:7], v[162:177]
	v_pk_mul_f32 v[146:147], v[98:99], v[16:17] op_sel_hi:[1,0]
	v_pk_mul_f32 v[148:149], v[100:101], v[16:17] op_sel_hi:[1,0]
	v_pk_mul_f32 v[150:151], v[102:103], v[16:17] op_sel_hi:[1,0]
	v_pk_mul_f32 v[152:153], v[104:105], v[16:17] op_sel_hi:[1,0]
	v_pk_mul_f32 v[154:155], v[106:107], v[16:17] op_sel_hi:[1,0]
	v_pk_mul_f32 v[156:157], v[108:109], v[16:17] op_sel_hi:[1,0]
	v_pk_mul_f32 v[158:159], v[110:111], v[16:17] op_sel_hi:[1,0]
	v_pk_mul_f32 v[160:161], v[112:113], v[16:17] op_sel_hi:[1,0]
	s_nop 1
	v_mfma_f32_32x32x16_f16 v[146:161], v[118:121], v[4:7], v[146:161]
	v_cvt_pk_f16_f32 v12, v50, v51
	v_cvt_pk_f16_f32 v13, v52, v53
	v_cvt_pk_f16_f32 v14, v54, v55
	v_cvt_pk_f16_f32 v15, v56, v57
	v_mfma_f32_32x32x16_f16 v[162:177], v[122:125], v[8:11], v[162:177]
	v_cvt_pk_f16_f32 v252, v58, v59
	v_cvt_pk_f16_f32 v253, v60, v61
	v_cvt_pk_f16_f32 v254, v62, v63
	v_cvt_pk_f16_f32 v255, v64, v65
	v_mfma_f32_32x32x16_f16 v[146:161], v[126:129], v[8:11], v[146:161]
	ds_read_b128 v[82:85], v246 offset:4096
	ds_read_b128 v[86:89], v246 offset:12288
	ds_read_b128 v[90:93], v246 offset:5120
	ds_read_b128 v[94:97], v246 offset:13312
	s_waitcnt lgkmcnt(4)
	v_mfma_f32_32x32x16_f16 v[162:177], v[130:133], v[12:15], v[162:177]
	v_cvt_pk_f16_f32 v4, v34, v35
	v_cvt_pk_f16_f32 v5, v36, v37
	v_mfma_f32_32x32x16_f16 v[146:161], v[134:137], v[12:15], v[146:161]
	v_cvt_pk_f16_f32 v6, v38, v39
	v_cvt_pk_f16_f32 v7, v40, v41
	v_mfma_f32_32x32x16_f16 v[162:177], v[138:141], v[252:255], v[162:177]
	v_cvt_pk_f16_f32 v8, v42, v43
	v_cvt_pk_f16_f32 v9, v44, v45
	v_mfma_f32_32x32x16_f16 v[146:161], v[142:145], v[252:255], v[146:161]
	v_cvt_pk_f16_f32 v10, v46, v47
	v_cvt_pk_f16_f32 v11, v48, v49
	ds_read_b128 v[98:101], v246 offset:6144
	ds_read_b128 v[102:105], v246 offset:14336
	ds_read_b128 v[106:109], v246 offset:7168
	ds_read_b128 v[110:113], v246 offset:15360
	s_waitcnt lgkmcnt(4)
	v_mfma_f32_32x32x16_f16 v[162:177], v[82:85], v[4:7], v[162:177]
	v_cvt_pk_f16_f32 v12, v18, v19
	v_cvt_pk_f16_f32 v13, v20, v21
	v_mfma_f32_32x32x16_f16 v[146:161], v[86:89], v[4:7], v[146:161]
	v_cvt_pk_f16_f32 v14, v22, v23
	v_cvt_pk_f16_f32 v15, v24, v25
	v_mfma_f32_32x32x16_f16 v[162:177], v[90:93], v[8:11], v[162:177]
	v_cvt_pk_f16_f32 v252, v26, v27
	v_cvt_pk_f16_f32 v253, v28, v29
	v_mfma_f32_32x32x16_f16 v[146:161], v[94:97], v[8:11], v[146:161]
	v_cvt_pk_f16_f32 v254, v30, v31
	v_cvt_pk_f16_f32 v255, v32, v33
	ds_read_b128 v[18:21], v246 offset:16384
	ds_read_b128 v[22:25], v246 offset:17408
	ds_read_b128 v[26:29], v246 offset:18432
	ds_read_b128 v[30:33], v246 offset:19456
	s_waitcnt lgkmcnt(4)
	v_mfma_f32_32x32x16_f16 v[162:177], v[98:101], v[12:15], v[162:177]
	v_mfma_f32_32x32x16_f16 v[146:161], v[102:105], v[12:15], v[146:161]
	v_mfma_f32_32x32x16_f16 v[162:177], v[106:109], v[252:255], v[162:177]
	v_mfma_f32_32x32x16_f16 v[146:161], v[110:113], v[252:255], v[146:161]
	ds_read_b128 v[130:133], v247 offset:33024
	ds_read_b128 v[134:137], v247 offset:33040
	ds_read_b128 v[138:141], v247 offset:33056
	ds_read_b128 v[142:145], v247 offset:33072
	ds_read_b128 v[114:117], v247 offset:33088
	ds_read_b128 v[118:121], v247 offset:33104
	ds_read_b128 v[122:125], v247 offset:33120
	ds_read_b128 v[126:129], v247 offset:33136
	s_nop 2
	v_cvt_pk_f16_f32 v4, v162, v163
	v_cvt_pk_f16_f32 v5, v164, v165
	v_cvt_pk_f16_f32 v6, v166, v167
	v_cvt_pk_f16_f32 v7, v168, v169
	v_cvt_pk_f16_f32 v8, v170, v171
	v_cvt_pk_f16_f32 v9, v172, v173
	v_cvt_pk_f16_f32 v10, v174, v175
	v_cvt_pk_f16_f32 v11, v176, v177
	v_cvt_pk_f16_f32 v12, v146, v147
	v_cvt_pk_f16_f32 v13, v148, v149
	v_cvt_pk_f16_f32 v14, v150, v151
	v_cvt_pk_f16_f32 v15, v152, v153
	v_cvt_pk_f16_f32 v252, v154, v155
	v_cvt_pk_f16_f32 v253, v156, v157
	v_cvt_pk_f16_f32 v254, v158, v159
	v_cvt_pk_f16_f32 v255, v160, v161
	s_waitcnt lgkmcnt(4)
	ds_read_b128 v[34:37], v246 offset:20480
	ds_read_b128 v[38:41], v246 offset:21504
	ds_read_b128 v[42:45], v246 offset:22528
	ds_read_b128 v[46:49], v246 offset:23552
	v_mfma_f32_32x32x16_f16 v[130:145], v[18:21], v[4:7], v[130:145]
	v_mfma_f32_32x32x16_f16 v[130:145], v[22:25], v[8:11], v[130:145]
	v_mfma_f32_32x32x16_f16 v[130:145], v[26:29], v[12:15], v[130:145]
	v_mfma_f32_32x32x16_f16 v[130:145], v[30:33], v[252:255], v[130:145]
	ds_read_b128 v[146:149], v247 offset:33536
	ds_read_b128 v[150:153], v247 offset:33552
	ds_read_b128 v[154:157], v247 offset:33568
	ds_read_b128 v[158:161], v247 offset:33584
	s_waitcnt lgkmcnt(4)
	ds_read_b128 v[98:101], v247 offset:33152
	ds_read_b128 v[102:105], v247 offset:33168
	ds_read_b128 v[106:109], v247 offset:33184
	ds_read_b128 v[110:113], v247 offset:33200
	ds_read_b128 v[50:53], v246 offset:24576
	ds_read_b128 v[54:57], v246 offset:25600
	ds_read_b128 v[58:61], v246 offset:26624
	ds_read_b128 v[62:65], v246 offset:27648
	v_mfma_f32_32x32x16_f16 v[114:129], v[34:37], v[4:7], v[114:129]
	v_exp_f32_e32 v130, v130
	v_exp_f32_e32 v131, v131
	v_exp_f32_e32 v132, v132
	v_exp_f32_e32 v133, v133
	v_exp_f32_e32 v134, v134
	v_exp_f32_e32 v135, v135
	v_exp_f32_e32 v136, v136
	v_exp_f32_e32 v137, v137
	v_mfma_f32_32x32x16_f16 v[114:129], v[38:41], v[8:11], v[114:129]
	v_exp_f32_e32 v138, v138
	v_exp_f32_e32 v139, v139
	v_exp_f32_e32 v140, v140
	v_exp_f32_e32 v141, v141
	v_exp_f32_e32 v142, v142
	v_exp_f32_e32 v143, v143
	v_exp_f32_e32 v144, v144
	v_exp_f32_e32 v145, v145
	v_mfma_f32_32x32x16_f16 v[114:129], v[42:45], v[12:15], v[114:129]
	v_pk_add_f32 v[130:131], v[130:131], s[82:83]
	v_pk_add_f32 v[132:133], v[132:133], s[82:83]
	v_pk_add_f32 v[134:135], v[134:135], s[82:83]
	v_pk_add_f32 v[136:137], v[136:137], s[82:83]
	v_pk_add_f32 v[138:139], v[138:139], s[82:83]
	v_pk_add_f32 v[140:141], v[140:141], s[82:83]
	v_pk_add_f32 v[142:143], v[142:143], s[82:83]
	v_pk_add_f32 v[144:145], v[144:145], s[82:83]
	v_mfma_f32_32x32x16_f16 v[114:129], v[46:49], v[252:255], v[114:129]
	v_rcp_f32_e32 v130, v130
	v_rcp_f32_e32 v131, v131
	v_rcp_f32_e32 v132, v132
	v_rcp_f32_e32 v133, v133
	v_rcp_f32_e32 v134, v134
	v_rcp_f32_e32 v135, v135
	v_rcp_f32_e32 v136, v136
	v_rcp_f32_e32 v137, v137
	v_rcp_f32_e32 v138, v138
	v_rcp_f32_e32 v139, v139
	v_rcp_f32_e32 v140, v140
	v_rcp_f32_e32 v141, v141
	v_rcp_f32_e32 v142, v142
	v_rcp_f32_e32 v143, v143
	v_rcp_f32_e32 v144, v144
	v_rcp_f32_e32 v145, v145
	s_waitcnt lgkmcnt(8)
	ds_read_b128 v[162:165], v247 offset:33600
	ds_read_b128 v[166:169], v247 offset:33616
	ds_read_b128 v[170:173], v247 offset:33632
	ds_read_b128 v[174:177], v247 offset:33648
	v_mul_f32_e32 v3, v146, v130
	v_mul_f32_e32 v16, v147, v131
	v_mul_f32_e32 v17, v148, v132
	v_fmac_f32_e32 v3, v149, v133
	v_fmac_f32_e32 v16, v150, v134
	v_fmac_f32_e32 v17, v151, v135
	v_fmac_f32_e32 v3, v152, v136
	v_fmac_f32_e32 v16, v153, v137
	v_fmac_f32_e32 v17, v154, v138
	v_fmac_f32_e32 v3, v155, v139
	v_fmac_f32_e32 v16, v156, v140
	v_fmac_f32_e32 v17, v157, v141
	v_fmac_f32_e32 v3, v158, v142
	v_fmac_f32_e32 v16, v159, v143
	v_fmac_f32_e32 v17, v160, v144
	v_fmac_f32_e32 v3, v161, v145
	s_waitcnt lgkmcnt(4)
	ds_read_b128 v[82:85], v247 offset:33216
	ds_read_b128 v[86:89], v247 offset:33232
	ds_read_b128 v[90:93], v247 offset:33248
	ds_read_b128 v[94:97], v247 offset:33264
	ds_read_b128 v[66:69], v246 offset:28672
	ds_read_b128 v[70:73], v246 offset:29696
	ds_read_b128 v[74:77], v246 offset:30720
	ds_read_b128 v[78:81], v246 offset:31744
	v_mfma_f32_32x32x16_f16 v[98:113], v[50:53], v[4:7], v[98:113]
	v_exp_f32_e32 v114, v114
	v_exp_f32_e32 v115, v115
	v_exp_f32_e32 v116, v116
	v_exp_f32_e32 v117, v117
	v_exp_f32_e32 v118, v118
	v_exp_f32_e32 v119, v119
	v_exp_f32_e32 v120, v120
	v_exp_f32_e32 v121, v121
	v_mfma_f32_32x32x16_f16 v[98:113], v[54:57], v[8:11], v[98:113]
	v_exp_f32_e32 v122, v122
	v_exp_f32_e32 v123, v123
	v_exp_f32_e32 v124, v124
	v_exp_f32_e32 v125, v125
	v_exp_f32_e32 v126, v126
	v_exp_f32_e32 v127, v127
	v_exp_f32_e32 v128, v128
	v_exp_f32_e32 v129, v129
	v_mfma_f32_32x32x16_f16 v[98:113], v[58:61], v[12:15], v[98:113]
	v_pk_add_f32 v[114:115], v[114:115], s[82:83]
	v_pk_add_f32 v[116:117], v[116:117], s[82:83]
	v_pk_add_f32 v[118:119], v[118:119], s[82:83]
	v_pk_add_f32 v[120:121], v[120:121], s[82:83]
	v_pk_add_f32 v[122:123], v[122:123], s[82:83]
	v_pk_add_f32 v[124:125], v[124:125], s[82:83]
	v_pk_add_f32 v[126:127], v[126:127], s[82:83]
	v_pk_add_f32 v[128:129], v[128:129], s[82:83]
	v_mfma_f32_32x32x16_f16 v[98:113], v[62:65], v[252:255], v[98:113]
	v_rcp_f32_e32 v114, v114
	v_rcp_f32_e32 v115, v115
	v_rcp_f32_e32 v116, v116
	v_rcp_f32_e32 v117, v117
	v_rcp_f32_e32 v118, v118
	v_rcp_f32_e32 v119, v119
	v_rcp_f32_e32 v120, v120
	v_rcp_f32_e32 v121, v121
	v_rcp_f32_e32 v122, v122
	v_rcp_f32_e32 v123, v123
	v_rcp_f32_e32 v124, v124
	v_rcp_f32_e32 v125, v125
	v_rcp_f32_e32 v126, v126
	v_rcp_f32_e32 v127, v127
	v_rcp_f32_e32 v128, v128
	v_rcp_f32_e32 v129, v129
	s_waitcnt lgkmcnt(8)
	ds_read_b128 v[18:21], v247 offset:33664
	ds_read_b128 v[22:25], v247 offset:33680
	ds_read_b128 v[26:29], v247 offset:33696
	ds_read_b128 v[30:33], v247 offset:33712
	v_fmac_f32_e32 v3, v162, v114
	v_fmac_f32_e32 v16, v163, v115
	v_fmac_f32_e32 v17, v164, v116
	v_fmac_f32_e32 v3, v165, v117
	v_fmac_f32_e32 v16, v166, v118
	v_fmac_f32_e32 v17, v167, v119
	v_fmac_f32_e32 v3, v168, v120
	v_fmac_f32_e32 v16, v169, v121
	v_fmac_f32_e32 v17, v170, v122
	v_fmac_f32_e32 v3, v171, v123
	v_fmac_f32_e32 v16, v172, v124
	v_fmac_f32_e32 v17, v173, v125
	v_fmac_f32_e32 v3, v174, v126
	v_fmac_f32_e32 v16, v175, v127
	v_fmac_f32_e32 v17, v176, v128
	v_fmac_f32_e32 v3, v177, v129
	s_waitcnt lgkmcnt(4)
	ds_read_b128 v[146:149], v247 offset:33728
	ds_read_b128 v[150:153], v247 offset:33744
	ds_read_b128 v[154:157], v247 offset:33760
	ds_read_b128 v[158:161], v247 offset:33776
	v_mfma_f32_32x32x16_f16 v[82:97], v[66:69], v[4:7], v[82:97]
	v_exp_f32_e32 v98, v98
	v_exp_f32_e32 v99, v99
	v_exp_f32_e32 v100, v100
	v_exp_f32_e32 v101, v101
	v_exp_f32_e32 v102, v102
	v_exp_f32_e32 v103, v103
	v_exp_f32_e32 v104, v104
	v_exp_f32_e32 v105, v105
	v_mfma_f32_32x32x16_f16 v[82:97], v[70:73], v[8:11], v[82:97]
	v_exp_f32_e32 v106, v106
	v_exp_f32_e32 v107, v107
	v_exp_f32_e32 v108, v108
	v_exp_f32_e32 v109, v109
	v_exp_f32_e32 v110, v110
	v_exp_f32_e32 v111, v111
	v_exp_f32_e32 v112, v112
	v_exp_f32_e32 v113, v113
	v_mfma_f32_32x32x16_f16 v[82:97], v[74:77], v[12:15], v[82:97]
	v_pk_add_f32 v[98:99], v[98:99], s[82:83]
	v_pk_add_f32 v[100:101], v[100:101], s[82:83]
	v_pk_add_f32 v[102:103], v[102:103], s[82:83]
	v_pk_add_f32 v[104:105], v[104:105], s[82:83]
	v_pk_add_f32 v[106:107], v[106:107], s[82:83]
	v_pk_add_f32 v[108:109], v[108:109], s[82:83]
	v_pk_add_f32 v[110:111], v[110:111], s[82:83]
	v_pk_add_f32 v[112:113], v[112:113], s[82:83]
	v_mfma_f32_32x32x16_f16 v[82:97], v[78:81], v[252:255], v[82:97]
	v_rcp_f32_e32 v98, v98
	v_rcp_f32_e32 v99, v99
	v_rcp_f32_e32 v100, v100
	v_rcp_f32_e32 v101, v101
	v_rcp_f32_e32 v102, v102
	v_rcp_f32_e32 v103, v103
	v_rcp_f32_e32 v104, v104
	v_rcp_f32_e32 v105, v105
	v_rcp_f32_e32 v106, v106
	v_rcp_f32_e32 v107, v107
	v_rcp_f32_e32 v108, v108
	v_rcp_f32_e32 v109, v109
	v_rcp_f32_e32 v110, v110
	v_rcp_f32_e32 v111, v111
	v_rcp_f32_e32 v112, v112
	v_rcp_f32_e32 v113, v113
	s_waitcnt lgkmcnt(4)
	v_fmac_f32_e32 v3, v18, v98
	v_fmac_f32_e32 v16, v19, v99
	v_fmac_f32_e32 v17, v20, v100
	v_fmac_f32_e32 v3, v21, v101
	v_fmac_f32_e32 v16, v22, v102
	v_fmac_f32_e32 v17, v23, v103
	v_fmac_f32_e32 v3, v24, v104
	v_fmac_f32_e32 v16, v25, v105
	v_fmac_f32_e32 v17, v26, v106
	v_fmac_f32_e32 v3, v27, v107
	v_fmac_f32_e32 v16, v28, v108
	v_fmac_f32_e32 v17, v29, v109
	v_fmac_f32_e32 v3, v30, v110
	v_fmac_f32_e32 v16, v31, v111
	v_fmac_f32_e32 v17, v32, v112
	v_fmac_f32_e32 v3, v33, v113
	v_exp_f32_e32 v82, v82
	v_exp_f32_e32 v83, v83
	v_exp_f32_e32 v84, v84
	v_exp_f32_e32 v85, v85
	v_exp_f32_e32 v86, v86
	v_exp_f32_e32 v87, v87
	v_exp_f32_e32 v88, v88
	v_exp_f32_e32 v89, v89
	v_exp_f32_e32 v90, v90
	v_exp_f32_e32 v91, v91
	v_exp_f32_e32 v92, v92
	v_exp_f32_e32 v93, v93
	v_exp_f32_e32 v94, v94
	v_exp_f32_e32 v95, v95
	v_exp_f32_e32 v96, v96
	v_exp_f32_e32 v97, v97
	v_pk_add_f32 v[82:83], v[82:83], s[82:83]
	v_pk_add_f32 v[84:85], v[84:85], s[82:83]
	v_pk_add_f32 v[86:87], v[86:87], s[82:83]
	v_pk_add_f32 v[88:89], v[88:89], s[82:83]
	v_pk_add_f32 v[90:91], v[90:91], s[82:83]
	v_pk_add_f32 v[92:93], v[92:93], s[82:83]
	v_pk_add_f32 v[94:95], v[94:95], s[82:83]
	v_pk_add_f32 v[96:97], v[96:97], s[82:83]
	v_rcp_f32_e32 v82, v82
	v_rcp_f32_e32 v83, v83
	v_rcp_f32_e32 v84, v84
	v_rcp_f32_e32 v85, v85
	v_rcp_f32_e32 v86, v86
	v_rcp_f32_e32 v87, v87
	v_rcp_f32_e32 v88, v88
	v_rcp_f32_e32 v89, v89
	v_rcp_f32_e32 v90, v90
	v_rcp_f32_e32 v91, v91
	v_rcp_f32_e32 v92, v92
	v_rcp_f32_e32 v93, v93
	v_rcp_f32_e32 v94, v94
	v_rcp_f32_e32 v95, v95
	v_rcp_f32_e32 v96, v96
	v_rcp_f32_e32 v97, v97
	s_waitcnt lgkmcnt(0)
	v_fmac_f32_e32 v3, v146, v82
	v_fmac_f32_e32 v16, v147, v83
	v_fmac_f32_e32 v17, v148, v84
	v_fmac_f32_e32 v3, v149, v85
	v_fmac_f32_e32 v16, v150, v86
	v_fmac_f32_e32 v17, v151, v87
	v_fmac_f32_e32 v3, v152, v88
	v_fmac_f32_e32 v16, v153, v89
	v_fmac_f32_e32 v17, v154, v90
	v_fmac_f32_e32 v3, v155, v91
	v_fmac_f32_e32 v16, v156, v92
	v_fmac_f32_e32 v17, v157, v93
	v_fmac_f32_e32 v3, v158, v94
	v_fmac_f32_e32 v16, v159, v95
	v_fmac_f32_e32 v17, v160, v96
	v_fmac_f32_e32 v3, v161, v97
	v_add_f32_e32 v3, v3, v16
	v_add_f32_e32 v3, v3, v17
	v_mov_b32_e32 v4, v3
	s_nop 1
	v_permlane32_swap_b32_e32 v4, v3
	s_and_saveexec_b64 s[8:9], s[10:11]
	s_cbranch_execz .LBB1_156
	s_waitcnt vmcnt(0)
	v_mul_f32_e32 v5, 0x40549a78, v238
	v_exp_f32_e32 v5, v5
	v_add_f32_e32 v3, v3, v4
	v_ashrrev_i32_e32 v7, 31, v235
	v_mov_b32_e32 v6, v235
	v_add_f32_e32 v3, v239, v3
	v_lshl_add_u64 v[6:7], v[6:7], 2, s[52:53]
	v_mul_f32_e32 v3, v5, v3
	global_store_dword v[6:7], v3, off
.LBB1_156:
	s_or_b64 exec, exec, s[8:9]
	v_add_u32_e32 v82, 1, v251
	v_cmp_ne_u32_e32 vcc, v82, v242
	s_mov_b64 s[10:11], 0
	v_mov_b32_e32 v251, v242
	s_and_saveexec_b64 s[8:9], vcc
	s_cbranch_execz .LBB1_147
	s_waitcnt lgkmcnt(0)
	v_add_u32_e32 v17, 32, v235
	v_cmp_gt_i32_e32 vcc, s17, v235
	v_mov_b32_e32 v238, 0
	v_readlane_b32 s20, v231, 31
	v_sub_u32_e32 v16, v231, v230
	s_and_saveexec_b64 s[10:11], vcc
	s_cbranch_execz .LBB1_146
	v_ashrrev_i32_e32 v5, 31, v17
	v_mov_b32_e32 v4, v17
	v_lshl_add_u64 v[4:5], v[4:5], 2, s[50:51]
	global_load_dword v238, v[4:5], off
	s_branch .LBB1_146
